# N1/FIN row-norm wave reduction via DPP + permlane swaps instead of six ds_bpermute hops (same pairing order), on top of v37
# speedup vs baseline: 1.0040x; 1.0040x over previous
.LBB0_221:
	v_pk_mul_f32 v[4:5], v[34:35], v[34:35]
	v_pk_mul_f32 v[6:7], v[32:33], v[32:33]
	v_pk_mul_f32 v[0:1], v[38:39], v[38:39]
	s_waitcnt lgkmcnt(0)
	v_pk_mul_f32 v[2:3], v[36:37], v[36:37]
	v_pk_mov_b32 v[8:9], v[6:7], v[4:5] op_sel:[1,0]
	v_mov_b32_e32 v7, v5
	v_pk_add_f32 v[4:5], v[8:9], v[6:7]
	v_pk_mov_b32 v[6:7], v[2:3], v[0:1] op_sel:[1,0]
	v_mov_b32_e32 v3, v1
	v_pk_add_f32 v[0:1], v[6:7], v[2:3]
	v_pk_add_f32 v[4:5], v[4:5], v[4:5] op_sel_hi:[0,1]
	v_pk_add_f32 v[0:1], v[0:1], v[0:1] op_sel_hi:[0,1]
	v_mul_f32_e32 v0, v40, v40
	v_pk_fma_f32 v[2:3], v[40:41], v[40:41], v[0:1] op_sel_hi:[1,1,0]
	v_mul_f32_e32 v0, v42, v42
	v_pk_fma_f32 v[6:7], v[42:43], v[42:43], v[0:1] op_sel_hi:[1,1,0]
	v_mul_f32_e32 v2, v28, v28
	v_mul_f32_e32 v6, v29, v29
	v_mul_f32_e32 v4, v30, v30
	v_mul_f32_e32 v0, v31, v31
	v_pk_add_f32 v[2:3], v[2:3], v[6:7]
	v_pk_add_f32 v[0:1], v[4:5], v[0:1]
	s_andn2_b64 vcc, exec, s[14:15]
	v_pk_add_f32 v[0:1], v[2:3], v[0:1]
	v_lshl_add_u64 v[2:3], v[120:121], 0, s[16:17]
	v_add_f32_e32 v0, v0, v1
	s_nop 1
	v_add_f32_dpp v0, v0, v0 quad_perm:[1,0,3,2] row_mask:0xf bank_mask:0xf
	s_mov_b32 s10, s12
	s_nop 1
	v_add_f32_dpp v0, v0, v0 quad_perm:[2,3,0,1] row_mask:0xf bank_mask:0xf
	s_nop 1
	v_add_f32_dpp v0, v0, v0 row_half_mirror row_mask:0xf bank_mask:0xf
	s_nop 1
	v_add_f32_dpp v0, v0, v0 row_mirror row_mask:0xf bank_mask:0xf
	v_mov_b32_e32 v1, v0
	s_nop 1
	v_permlane16_swap_b32_e32 v0, v1
	v_add_f32_e32 v0, v0, v1
	v_mov_b32_e32 v1, v0
	s_nop 1
	v_permlane32_swap_b32_e32 v0, v1
	v_add_f32_e32 v0, v0, v1
	v_fmamk_f32 v0, v0, 0x3a800000, v200
	v_rsq_f32_e32 v0, v0
	s_nop 0
	v_pk_mul_f32 v[4:5], v[32:33], v[0:1] op_sel_hi:[1,0]
	v_pk_mul_f32 v[6:7], v[34:35], v[0:1] op_sel_hi:[1,0]
	v_pk_fma_f32 v[4:5], v[82:83], v[4:5], v[60:61]
	v_pk_mul_f32 v[8:9], v[36:37], v[0:1] op_sel_hi:[1,0]
	v_pk_mul_f32 v[10:11], v[38:39], v[0:1] op_sel_hi:[1,0]
	v_pk_fma_f32 v[6:7], v[84:85], v[6:7], v[62:63]
	v_cvt_pk_bf16_f32 v4, v4, v5
	v_pk_fma_f32 v[10:11], v[88:89], v[10:11], v[72:73]
	v_cvt_pk_bf16_f32 v5, v6, v7
	v_pk_fma_f32 v[8:9], v[86:87], v[8:9], v[70:71]
	global_store_dwordx2 v[2:3], v[4:5], off
	v_cvt_pk_bf16_f32 v4, v8, v9
	v_cvt_pk_bf16_f32 v5, v10, v11
	v_pk_mul_f32 v[12:13], v[40:41], v[0:1] op_sel_hi:[1,0]
	global_store_dwordx2 v[2:3], v[4:5], off offset:512
	v_pk_mul_f32 v[4:5], v[42:43], v[0:1] op_sel_hi:[1,0]
	v_pk_fma_f32 v[6:7], v[90:91], v[12:13], v[74:75]
	v_pk_fma_f32 v[4:5], v[92:93], v[4:5], v[76:77]
	v_cvt_pk_bf16_f32 v6, v6, v7
	v_cvt_pk_bf16_f32 v7, v4, v5
	v_pk_mul_f32 v[4:5], v[44:45], v[0:1] op_sel_hi:[1,0]
	v_pk_mul_f32 v[0:1], v[46:47], v[0:1] op_sel_hi:[1,0]
	v_pk_fma_f32 v[4:5], v[94:95], v[4:5], v[78:79]
	global_store_dwordx2 v[2:3], v[6:7], off offset:1024
	v_pk_fma_f32 v[0:1], v[96:97], v[0:1], v[80:81]
	v_cvt_pk_bf16_f32 v4, v4, v5
	v_cvt_pk_bf16_f32 v5, v0, v1
	global_store_dwordx2 v[2:3], v[4:5], off offset:1536
	s_waitcnt vmcnt(4)
	v_mov_b32_e32 v135, v136
	v_mov_b32_e32 v14, v112
	v_mov_b32_e32 v15, v113
	v_mov_b32_e32 v8, v106
	v_mov_b32_e32 v6, v104
	v_mov_b32_e32 v0, v98
	v_mov_b32_e32 v1, v99
	v_mov_b32_e32 v2, v100
	v_mov_b32_e32 v3, v101
	v_mov_b32_e32 v4, v102
	v_mov_b32_e32 v5, v103
	v_mov_b32_e32 v7, v105
	v_mov_b32_e32 v9, v107
	v_mov_b32_e32 v10, v108
	v_mov_b32_e32 v11, v109
	v_mov_b32_e32 v12, v110
	v_mov_b32_e32 v13, v111
	s_cbranch_vccz .LBB0_245

.LBB0_1569:
	v_pk_fma_f32 v[72:73], v[14:15], v[88:89], v[72:73]
	v_pk_fma_f32 v[66:67], v[12:13], v[86:87], v[66:67]
	v_pk_fma_f32 v[78:79], v[20:21], v[78:79], v[60:61]
	v_pk_fma_f32 v[74:75], v[24:25], v[74:75], v[58:59]
	v_pk_mul_f32 v[58:59], v[72:73], v[72:73]
	v_pk_mul_f32 v[60:61], v[66:67], v[66:67]
	v_pk_fma_f32 v[64:65], v[26:27], v[76:77], v[64:65]
	v_pk_mov_b32 v[76:77], v[60:61], v[58:59] op_sel:[1,0]
	v_mov_b32_e32 v61, v59
	v_pk_fma_f32 v[70:71], v[18:19], v[84:85], v[70:71]
	v_pk_fma_f32 v[62:63], v[16:17], v[82:83], v[62:63]
	v_pk_add_f32 v[58:59], v[76:77], v[60:61]
	v_pk_mul_f32 v[60:61], v[70:71], v[70:71]
	v_pk_add_f32 v[58:59], v[58:59], v[58:59] op_sel_hi:[0,1]
	v_pk_mul_f32 v[76:77], v[62:63], v[62:63]
	v_pk_fma_f32 v[68:69], v[22:23], v[80:81], v[68:69]
	v_pk_mov_b32 v[80:81], v[76:77], v[60:61] op_sel:[1,0]
	v_mov_b32_e32 v77, v61
	v_mul_f32_e32 v58, v78, v78
	v_pk_add_f32 v[60:61], v[80:81], v[76:77]
	v_pk_fma_f32 v[76:77], v[78:79], v[78:79], v[58:59] op_sel_hi:[1,1,0]
	v_mul_f32_e32 v58, v68, v68
	v_pk_add_f32 v[60:61], v[60:61], v[60:61] op_sel_hi:[0,1]
	v_pk_fma_f32 v[80:81], v[68:69], v[68:69], v[58:59] op_sel_hi:[1,1,0]
	v_mul_f32_e32 v76, v74, v74
	v_mul_f32_e32 v80, v75, v75
	v_mul_f32_e32 v58, v64, v64
	v_mul_f32_e32 v60, v65, v65
	v_pk_add_f32 v[76:77], v[76:77], v[80:81]
	v_pk_add_f32 v[58:59], v[58:59], v[60:61]
	s_and_b64 s[8:9], s[8:9], exec
	v_pk_add_f32 v[58:59], v[76:77], v[58:59]
	s_cselect_b32 s8, s17, 0xffffff00
	v_add_f32_e32 v58, v58, v59
	s_nop 1
	v_add_f32_dpp v58, v58, v58 quad_perm:[1,0,3,2] row_mask:0xf bank_mask:0xf
	s_add_i32 s8, s19, s8
	s_ashr_i32 s9, s8, 31
	s_lshl_b64 s[8:9], s[8:9], 12
	v_lshl_add_u64 v[80:81], v[54:55], 0, s[8:9]
	s_nop 1
	v_add_f32_dpp v58, v58, v58 quad_perm:[2,3,0,1] row_mask:0xf bank_mask:0xf
	s_and_b64 vcc, exec, s[6:7]
	s_waitcnt vmcnt(0)
	v_mov_b32_e32 v99, v100
	s_nop 1
	v_add_f32_dpp v58, v58, v58 row_half_mirror row_mask:0xf bank_mask:0xf
	s_nop 1
	v_add_f32_dpp v58, v58, v58 row_mirror row_mask:0xf bank_mask:0xf
	v_mov_b32_e32 v59, v58
	s_nop 1
	v_permlane16_swap_b32_e32 v58, v59
	v_add_f32_e32 v58, v58, v59
	v_mov_b32_e32 v59, v58
	s_nop 1
	v_permlane32_swap_b32_e32 v58, v59
	v_add_f32_e32 v58, v58, v59
	v_fmamk_f32 v58, v58, 0x3a800000, v92
	v_rsq_f32_e32 v76, v58
	s_nop 0
	v_pk_mul_f32 v[58:59], v[66:67], v[76:77] op_sel_hi:[1,0]
	v_pk_mul_f32 v[60:61], v[72:73], v[76:77] op_sel_hi:[1,0]
	v_pk_mul_f32 v[58:59], v[0:1], v[58:59]
	v_pk_mul_f32 v[60:61], v[2:3], v[60:61]
	global_store_dwordx4 v[80:81], v[58:61], off nt
	v_lshlrev_b32_e32 v66, 16, v140
	v_and_b32_e32 v67, 0xffff0000, v140
	v_pk_mul_f32 v[58:59], v[62:63], v[76:77] op_sel_hi:[1,0]
	v_pk_mul_f32 v[60:61], v[70:71], v[76:77] op_sel_hi:[1,0]
	v_pk_mul_f32 v[58:59], v[4:5], v[58:59]
	v_pk_mul_f32 v[60:61], v[6:7], v[60:61]
	global_store_dwordx4 v[80:81], v[58:61], off offset:1024 nt
	v_lshlrev_b32_e32 v72, 16, v141
	v_and_b32_e32 v73, 0xffff0000, v141
	v_pk_mul_f32 v[58:59], v[78:79], v[76:77] op_sel_hi:[1,0]
	v_pk_mul_f32 v[60:61], v[68:69], v[76:77] op_sel_hi:[1,0]
	v_pk_mul_f32 v[58:59], v[8:9], v[58:59]
	v_pk_mul_f32 v[60:61], v[10:11], v[60:61]
	global_store_dwordx4 v[80:81], v[58:61], off offset:2048 nt
	v_lshlrev_b32_e32 v62, 16, v142
	v_and_b32_e32 v63, 0xffff0000, v142
	v_pk_mul_f32 v[58:59], v[74:75], v[76:77] op_sel_hi:[1,0]
	v_pk_mul_f32 v[60:61], v[64:65], v[76:77] op_sel_hi:[1,0]
	v_pk_mul_f32 v[58:59], v[28:29], v[58:59]
	v_pk_mul_f32 v[60:61], v[30:31], v[60:61]
	global_store_dwordx4 v[80:81], v[58:61], off offset:3072 nt
	v_lshlrev_b32_e32 v70, 16, v143
	v_and_b32_e32 v71, 0xffff0000, v143
	v_lshlrev_b32_e32 v60, 16, v144
	v_and_b32_e32 v61, 0xffff0000, v144
	v_lshlrev_b32_e32 v68, 16, v145
	v_and_b32_e32 v69, 0xffff0000, v145
	v_lshlrev_b32_e32 v58, 16, v146
	v_and_b32_e32 v59, 0xffff0000, v146
	v_lshlrev_b32_e32 v64, 16, v147
	v_and_b32_e32 v65, 0xffff0000, v147
	s_cbranch_vccnz .LBB0_1579
